# speedup vs baseline: 1.0066x; 1.0053x over previous
_Z15qkv_proj_kernelPKDF16_S0_PKfS2_S2_PDF16_S3_S3_:
	s_lshr_b32 s4, s2, 2
	s_and_b32 s3, s2, 7
	s_and_b32 s22, s4, 8
	s_or_b32 s4, s22, s3
	v_readfirstlane_b32 s18, v0
	s_ashr_i32 s3, s2, 6
	s_lshl_b32 s21, s4, 8
	s_bfe_u32 s20, s2, 0x20003
	v_and_b32_e32 v1, 63, v0
	s_cmpk_lt_u32 s18, 0x200
	s_mulk_i32 s20, 0xc0
	s_cbranch_scc1 .LBB1_30
	s_load_dwordx4 s[4:7], s[0:1], 0x0
	s_sub_i32 s10, 2, s3
	s_lshr_b32 s12, s18, 6
	s_add_i32 s12, s12, -8
	s_mul_i32 s13, s10, 0x600000
	s_mul_hi_i32 s14, s10, 0x600000
	s_mul_i32 s15, s10, 0x120000
	s_waitcnt lgkmcnt(0)
	s_add_u32 s4, s4, s13
	s_addc_u32 s5, s5, s14
	s_add_u32 s6, s6, s15
	s_addc_u32 s7, s7, 0
	v_lshrrev_b32_e32 v2, 2, v1
	v_lshrrev_b32_e32 v3, 4, v1
	v_xor_b32_e32 v3, v3, v1
	v_and_b32_e32 v3, 3, v3
	v_lshlrev_b32_e32 v3, 4, v3
	v_mul_u32_u24_e32 v2, 0x600, v2
	v_add_u32_e32 v2, v2, v3
	s_mul_i32 s16, s12, 7
	s_mul_i32 s27, s20, 0x600
	s_add_u32 s6, s6, s27
	s_addc_u32 s7, s7, 0
	s_add_i32 s27, s21, -192
	s_mul_i32 s27, s27, 0x600
	s_ashr_i32 s28, s27, 31
	s_add_u32 s4, s4, s27
	s_addc_u32 s5, s5, s28
	s_add_i32 s17, s16, 0
	s_cmp_ge_u32 s17, 12
	s_cselect_b32 s24, s4, s6
	s_cselect_b32 s25, s5, s7
	s_mul_i32 s17, s17, 0x6000
	s_add_u32 s30, s24, s17
	s_addc_u32 s31, s25, 0
	s_add_i32 s17, s16, 1
	s_cmp_ge_u32 s17, 12
	s_cselect_b32 s24, s4, s6
	s_cselect_b32 s25, s5, s7
	s_mul_i32 s17, s17, 0x6000
	s_add_u32 s32, s24, s17
	s_addc_u32 s33, s25, 0
	s_add_i32 s17, s16, 2
	s_cmp_ge_u32 s17, 12
	s_cselect_b32 s24, s4, s6
	s_cselect_b32 s25, s5, s7
	s_mul_i32 s17, s17, 0x6000
	s_add_u32 s34, s24, s17
	s_addc_u32 s35, s25, 0
	s_add_i32 s17, s16, 3
	s_cmp_ge_u32 s17, 12
	s_cselect_b32 s24, s4, s6
	s_cselect_b32 s25, s5, s7
	s_mul_i32 s17, s17, 0x6000
	s_add_u32 s36, s24, s17
	s_addc_u32 s37, s25, 0
	s_add_i32 s17, s16, 4
	s_cmp_ge_u32 s17, 12
	s_cselect_b32 s24, s4, s6
	s_cselect_b32 s25, s5, s7
	s_mul_i32 s17, s17, 0x6000
	s_add_u32 s38, s24, s17
	s_addc_u32 s39, s25, 0
	s_add_i32 s17, s16, 5
	s_cmp_ge_u32 s17, 12
	s_cselect_b32 s24, s4, s6
	s_cselect_b32 s25, s5, s7
	s_mul_i32 s17, s17, 0x6000
	s_add_u32 s40, s24, s17
	s_addc_u32 s41, s25, 0
	s_add_i32 s17, s16, 6
	s_cmp_ge_u32 s17, 12
	s_cselect_b32 s24, s4, s6
	s_cselect_b32 s25, s5, s7
	s_mul_i32 s17, s17, 0x6000
	s_add_u32 s42, s24, s17
	s_addc_u32 s43, s25, 0
	s_mul_i32 s26, s12, 0x1c00
	s_lshl_b32 s11, s10, 3
	s_add_i32 s11, s11, 0x10
	s_load_dwordx2 s[8:9], s[0:1], s11
	s_cmp_eq_u32 s10, 0
	s_cselect_b32 s29, 0x3e38aa3b, 1.0
	v_lshl_add_u32 v19, s12, 6, v1
	v_lshlrev_b32_e32 v21, 2, v19
	v_add_u32_e32 v21, 0x23800, v21
	v_min_u32_e32 v19, 0xbf, v19
	v_add_u32_e32 v19, s20, v19
	v_lshlrev_b32_e32 v19, 2, v19
	s_waitcnt lgkmcnt(0)
	global_load_dword v20, v19, s[8:9]
	s_add_i32 m0, s26, 2048
	s_nop 0
	global_load_lds_dwordx4 v2, s[30:31]
	s_add_i32 m0, s26, 3072
	s_nop 0
	global_load_lds_dwordx4 v2, s[32:33]
	s_add_i32 m0, s26, 4096
	s_nop 0
	global_load_lds_dwordx4 v2, s[34:35]
	s_add_i32 m0, s26, 5120
	s_nop 0
	global_load_lds_dwordx4 v2, s[36:37]
	s_add_i32 m0, s26, 6144
	s_nop 0
	global_load_lds_dwordx4 v2, s[38:39]
	s_add_i32 m0, s26, 7168
	s_nop 0
	global_load_lds_dwordx4 v2, s[40:41]
	s_add_i32 m0, s26, 8192
	s_nop 0
	global_load_lds_dwordx4 v2, s[42:43]
	s_add_i32 m0, s26, 30656
	s_nop 0
	global_load_lds_dwordx4 v2, s[30:31] offset:64
	s_add_i32 m0, s26, 31680
	s_nop 0
	global_load_lds_dwordx4 v2, s[32:33] offset:64
	s_add_i32 m0, s26, 32704
	s_nop 0
	global_load_lds_dwordx4 v2, s[34:35] offset:64
	s_add_i32 m0, s26, 33728
	s_nop 0
	global_load_lds_dwordx4 v2, s[36:37] offset:64
	s_add_i32 m0, s26, 34752
	s_nop 0
	global_load_lds_dwordx4 v2, s[38:39] offset:64
	s_add_i32 m0, s26, 35776
	s_nop 0
	global_load_lds_dwordx4 v2, s[40:41] offset:64
	s_add_i32 m0, s26, 36800
	s_nop 0
	global_load_lds_dwordx4 v2, s[42:43] offset:64
	s_add_i32 m0, s26, 59264
	s_nop 0
	global_load_lds_dwordx4 v2, s[30:31] offset:128
	s_add_i32 m0, s26, 60288
	s_nop 0
	global_load_lds_dwordx4 v2, s[32:33] offset:128
	s_add_i32 m0, s26, 61312
	s_nop 0
	global_load_lds_dwordx4 v2, s[34:35] offset:128
	s_add_i32 m0, s26, 62336
	s_nop 0
	global_load_lds_dwordx4 v2, s[36:37] offset:128
	s_add_i32 m0, s26, 63360
	s_nop 0
	global_load_lds_dwordx4 v2, s[38:39] offset:128
	s_add_i32 m0, s26, 64384
	s_nop 0
	global_load_lds_dwordx4 v2, s[40:41] offset:128
	s_add_i32 m0, s26, 65408
	s_nop 0
	global_load_lds_dwordx4 v2, s[42:43] offset:128
	s_add_i32 m0, s26, 87872
	s_nop 0
	global_load_lds_dwordx4 v2, s[30:31] offset:192
	s_add_i32 m0, s26, 88896
	s_nop 0
	global_load_lds_dwordx4 v2, s[32:33] offset:192
	s_add_i32 m0, s26, 89920
	s_nop 0
	global_load_lds_dwordx4 v2, s[34:35] offset:192
	s_add_i32 m0, s26, 90944
	s_nop 0
	global_load_lds_dwordx4 v2, s[36:37] offset:192
	s_add_i32 m0, s26, 91968
	s_nop 0
	global_load_lds_dwordx4 v2, s[38:39] offset:192
	s_add_i32 m0, s26, 92992
	s_nop 0
	global_load_lds_dwordx4 v2, s[40:41] offset:192
	s_add_i32 m0, s26, 94016
	s_nop 0
	global_load_lds_dwordx4 v2, s[42:43] offset:192
	s_waitcnt vmcnt(21)
	v_mul_f32_e32 v20, s29, v20
	ds_write_b32 v21, v20
	s_waitcnt lgkmcnt(0)
	s_barrier
	s_add_i32 m0, s26, 116480
	s_nop 0
	global_load_lds_dwordx4 v2, s[30:31] offset:256
	s_add_i32 m0, s26, 117504
	s_nop 0
	global_load_lds_dwordx4 v2, s[32:33] offset:256
	s_add_i32 m0, s26, 118528
	s_nop 0
	global_load_lds_dwordx4 v2, s[34:35] offset:256
	s_add_i32 m0, s26, 119552
	s_nop 0
	global_load_lds_dwordx4 v2, s[36:37] offset:256
	s_add_i32 m0, s26, 120576
	s_nop 0
	global_load_lds_dwordx4 v2, s[38:39] offset:256
	s_add_i32 m0, s26, 121600
	s_nop 0
	global_load_lds_dwordx4 v2, s[40:41] offset:256
	s_add_i32 m0, s26, 122624
	s_nop 0
	global_load_lds_dwordx4 v2, s[42:43] offset:256
	s_waitcnt vmcnt(21)
	s_barrier
	s_add_i32 m0, s26, 1728
	s_nop 0
	global_load_lds_dwordx4 v2, s[30:31] offset:320
	s_add_i32 m0, s26, 2752
	s_nop 0
	global_load_lds_dwordx4 v2, s[32:33] offset:320
	s_add_i32 m0, s26, 3776
	s_nop 0
	global_load_lds_dwordx4 v2, s[34:35] offset:320
	s_add_i32 m0, s26, 4800
	s_nop 0
	global_load_lds_dwordx4 v2, s[36:37] offset:320
	s_add_i32 m0, s26, 5824
	s_nop 0
	global_load_lds_dwordx4 v2, s[38:39] offset:320
	s_add_i32 m0, s26, 6848
	s_nop 0
	global_load_lds_dwordx4 v2, s[40:41] offset:320
	s_add_i32 m0, s26, 7872
	s_nop 0
	global_load_lds_dwordx4 v2, s[42:43] offset:320
	s_waitcnt vmcnt(21)
	s_barrier
	s_add_i32 m0, s26, 30336
	s_nop 0
	global_load_lds_dwordx4 v2, s[30:31] offset:384
	s_add_i32 m0, s26, 31360
	s_nop 0
	global_load_lds_dwordx4 v2, s[32:33] offset:384
	s_add_i32 m0, s26, 32384
	s_nop 0
	global_load_lds_dwordx4 v2, s[34:35] offset:384
	s_add_i32 m0, s26, 33408
	s_nop 0
	global_load_lds_dwordx4 v2, s[36:37] offset:384
	s_add_i32 m0, s26, 34432
	s_nop 0
	global_load_lds_dwordx4 v2, s[38:39] offset:384
	s_add_i32 m0, s26, 35456
	s_nop 0
	global_load_lds_dwordx4 v2, s[40:41] offset:384
	s_add_i32 m0, s26, 36480
	s_nop 0
	global_load_lds_dwordx4 v2, s[42:43] offset:384
	s_waitcnt vmcnt(21)
	s_barrier
	s_add_i32 m0, s26, 58944
	s_nop 0
	global_load_lds_dwordx4 v2, s[30:31] offset:448
	s_add_i32 m0, s26, 59968
	s_nop 0
	global_load_lds_dwordx4 v2, s[32:33] offset:448
	s_add_i32 m0, s26, 60992
	s_nop 0
	global_load_lds_dwordx4 v2, s[34:35] offset:448
	s_add_i32 m0, s26, 62016
	s_nop 0
	global_load_lds_dwordx4 v2, s[36:37] offset:448
	s_add_i32 m0, s26, 63040
	s_nop 0
	global_load_lds_dwordx4 v2, s[38:39] offset:448
	s_add_i32 m0, s26, 64064
	s_nop 0
	global_load_lds_dwordx4 v2, s[40:41] offset:448
	s_add_i32 m0, s26, 65088
	s_nop 0
	global_load_lds_dwordx4 v2, s[42:43] offset:448
	s_waitcnt vmcnt(21)
	s_barrier
	s_add_i32 m0, s26, 87552
	s_nop 0
	global_load_lds_dwordx4 v2, s[30:31] offset:512
	s_add_i32 m0, s26, 88576
	s_nop 0
	global_load_lds_dwordx4 v2, s[32:33] offset:512
	s_add_i32 m0, s26, 89600
	s_nop 0
	global_load_lds_dwordx4 v2, s[34:35] offset:512
	s_add_i32 m0, s26, 90624
	s_nop 0
	global_load_lds_dwordx4 v2, s[36:37] offset:512
	s_add_i32 m0, s26, 91648
	s_nop 0
	global_load_lds_dwordx4 v2, s[38:39] offset:512
	s_add_i32 m0, s26, 92672
	s_nop 0
	global_load_lds_dwordx4 v2, s[40:41] offset:512
	s_add_i32 m0, s26, 93696
	s_nop 0
	global_load_lds_dwordx4 v2, s[42:43] offset:512
	s_waitcnt vmcnt(21)
	s_barrier
	s_add_i32 m0, s26, 116160
	s_nop 0
	global_load_lds_dwordx4 v2, s[30:31] offset:576
	s_add_i32 m0, s26, 117184
	s_nop 0
	global_load_lds_dwordx4 v2, s[32:33] offset:576
	s_add_i32 m0, s26, 118208
	s_nop 0
	global_load_lds_dwordx4 v2, s[34:35] offset:576
	s_add_i32 m0, s26, 119232
	s_nop 0
	global_load_lds_dwordx4 v2, s[36:37] offset:576
	s_add_i32 m0, s26, 120256
	s_nop 0
	global_load_lds_dwordx4 v2, s[38:39] offset:576
	s_add_i32 m0, s26, 121280
	s_nop 0
	global_load_lds_dwordx4 v2, s[40:41] offset:576
	s_add_i32 m0, s26, 122304
	s_nop 0
	global_load_lds_dwordx4 v2, s[42:43] offset:576
	s_waitcnt vmcnt(21)
	s_barrier
	s_add_i32 m0, s26, 1408
	s_nop 0
	global_load_lds_dwordx4 v2, s[30:31] offset:640
	s_add_i32 m0, s26, 2432
	s_nop 0
	global_load_lds_dwordx4 v2, s[32:33] offset:640
	s_add_i32 m0, s26, 3456
	s_nop 0
	global_load_lds_dwordx4 v2, s[34:35] offset:640
	s_add_i32 m0, s26, 4480
	s_nop 0
	global_load_lds_dwordx4 v2, s[36:37] offset:640
	s_add_i32 m0, s26, 5504
	s_nop 0
	global_load_lds_dwordx4 v2, s[38:39] offset:640
	s_add_i32 m0, s26, 6528
	s_nop 0
	global_load_lds_dwordx4 v2, s[40:41] offset:640
	s_add_i32 m0, s26, 7552
	s_nop 0
	global_load_lds_dwordx4 v2, s[42:43] offset:640
	s_waitcnt vmcnt(21)
	s_barrier
	s_add_i32 m0, s26, 30016
	s_nop 0
	global_load_lds_dwordx4 v2, s[30:31] offset:704
	s_add_i32 m0, s26, 31040
	s_nop 0
	global_load_lds_dwordx4 v2, s[32:33] offset:704
	s_add_i32 m0, s26, 32064
	s_nop 0
	global_load_lds_dwordx4 v2, s[34:35] offset:704
	s_add_i32 m0, s26, 33088
	s_nop 0
	global_load_lds_dwordx4 v2, s[36:37] offset:704
	s_add_i32 m0, s26, 34112
	s_nop 0
	global_load_lds_dwordx4 v2, s[38:39] offset:704
	s_add_i32 m0, s26, 35136
	s_nop 0
	global_load_lds_dwordx4 v2, s[40:41] offset:704
	s_add_i32 m0, s26, 36160
	s_nop 0
	global_load_lds_dwordx4 v2, s[42:43] offset:704
	s_waitcnt vmcnt(21)
	s_barrier
	s_add_i32 m0, s26, 58624
	s_nop 0
	global_load_lds_dwordx4 v2, s[30:31] offset:768
	s_add_i32 m0, s26, 59648
	s_nop 0
	global_load_lds_dwordx4 v2, s[32:33] offset:768
	s_add_i32 m0, s26, 60672
	s_nop 0
	global_load_lds_dwordx4 v2, s[34:35] offset:768
	s_add_i32 m0, s26, 61696
	s_nop 0
	global_load_lds_dwordx4 v2, s[36:37] offset:768
	s_add_i32 m0, s26, 62720
	s_nop 0
	global_load_lds_dwordx4 v2, s[38:39] offset:768
	s_add_i32 m0, s26, 63744
	s_nop 0
	global_load_lds_dwordx4 v2, s[40:41] offset:768
	s_add_i32 m0, s26, 64768
	s_nop 0
	global_load_lds_dwordx4 v2, s[42:43] offset:768
	s_waitcnt vmcnt(21)
	s_barrier
	s_add_i32 m0, s26, 87232
	s_nop 0
	global_load_lds_dwordx4 v2, s[30:31] offset:832
	s_add_i32 m0, s26, 88256
	s_nop 0
	global_load_lds_dwordx4 v2, s[32:33] offset:832
	s_add_i32 m0, s26, 89280
	s_nop 0
	global_load_lds_dwordx4 v2, s[34:35] offset:832
	s_add_i32 m0, s26, 90304
	s_nop 0
	global_load_lds_dwordx4 v2, s[36:37] offset:832
	s_add_i32 m0, s26, 91328
	s_nop 0
	global_load_lds_dwordx4 v2, s[38:39] offset:832
	s_add_i32 m0, s26, 92352
	s_nop 0
	global_load_lds_dwordx4 v2, s[40:41] offset:832
	s_add_i32 m0, s26, 93376
	s_nop 0
	global_load_lds_dwordx4 v2, s[42:43] offset:832
	s_waitcnt vmcnt(21)
	s_barrier
	s_add_i32 m0, s26, 115840
	s_nop 0
	global_load_lds_dwordx4 v2, s[30:31] offset:896
	s_add_i32 m0, s26, 116864
	s_nop 0
	global_load_lds_dwordx4 v2, s[32:33] offset:896
	s_add_i32 m0, s26, 117888
	s_nop 0
	global_load_lds_dwordx4 v2, s[34:35] offset:896
	s_add_i32 m0, s26, 118912
	s_nop 0
	global_load_lds_dwordx4 v2, s[36:37] offset:896
	s_add_i32 m0, s26, 119936
	s_nop 0
	global_load_lds_dwordx4 v2, s[38:39] offset:896
	s_add_i32 m0, s26, 120960
	s_nop 0
	global_load_lds_dwordx4 v2, s[40:41] offset:896
	s_add_i32 m0, s26, 121984
	s_nop 0
	global_load_lds_dwordx4 v2, s[42:43] offset:896
	s_waitcnt vmcnt(21)
	s_barrier
	s_add_i32 m0, s26, 1088
	s_nop 0
	global_load_lds_dwordx4 v2, s[30:31] offset:960
	s_add_i32 m0, s26, 2112
	s_nop 0
	global_load_lds_dwordx4 v2, s[32:33] offset:960
	s_add_i32 m0, s26, 3136
	s_nop 0
	global_load_lds_dwordx4 v2, s[34:35] offset:960
	s_add_i32 m0, s26, 4160
	s_nop 0
	global_load_lds_dwordx4 v2, s[36:37] offset:960
	s_add_i32 m0, s26, 5184
	s_nop 0
	global_load_lds_dwordx4 v2, s[38:39] offset:960
	s_add_i32 m0, s26, 6208
	s_nop 0
	global_load_lds_dwordx4 v2, s[40:41] offset:960
	s_add_i32 m0, s26, 7232
	s_nop 0
	global_load_lds_dwordx4 v2, s[42:43] offset:960
	s_waitcnt vmcnt(21)
	s_barrier
	s_add_i32 m0, s26, 29696
	s_nop 0
	global_load_lds_dwordx4 v2, s[30:31] offset:1024
	s_add_i32 m0, s26, 30720
	s_nop 0
	global_load_lds_dwordx4 v2, s[32:33] offset:1024
	s_add_i32 m0, s26, 31744
	s_nop 0
	global_load_lds_dwordx4 v2, s[34:35] offset:1024
	s_add_i32 m0, s26, 32768
	s_nop 0
	global_load_lds_dwordx4 v2, s[36:37] offset:1024
	s_add_i32 m0, s26, 33792
	s_nop 0
	global_load_lds_dwordx4 v2, s[38:39] offset:1024
	s_add_i32 m0, s26, 34816
	s_nop 0
	global_load_lds_dwordx4 v2, s[40:41] offset:1024
	s_add_i32 m0, s26, 35840
	s_nop 0
	global_load_lds_dwordx4 v2, s[42:43] offset:1024
	s_waitcnt vmcnt(21)
	s_barrier
	s_add_i32 m0, s26, 58304
	s_nop 0
	global_load_lds_dwordx4 v2, s[30:31] offset:1088
	s_add_i32 m0, s26, 59328
	s_nop 0
	global_load_lds_dwordx4 v2, s[32:33] offset:1088
	s_add_i32 m0, s26, 60352
	s_nop 0
	global_load_lds_dwordx4 v2, s[34:35] offset:1088
	s_add_i32 m0, s26, 61376
	s_nop 0
	global_load_lds_dwordx4 v2, s[36:37] offset:1088
	s_add_i32 m0, s26, 62400
	s_nop 0
	global_load_lds_dwordx4 v2, s[38:39] offset:1088
	s_add_i32 m0, s26, 63424
	s_nop 0
	global_load_lds_dwordx4 v2, s[40:41] offset:1088
	s_add_i32 m0, s26, 64448
	s_nop 0
	global_load_lds_dwordx4 v2, s[42:43] offset:1088
	s_waitcnt vmcnt(21)
	s_barrier
	s_add_i32 m0, s26, 86912
	s_nop 0
	global_load_lds_dwordx4 v2, s[30:31] offset:1152
	s_add_i32 m0, s26, 87936
	s_nop 0
	global_load_lds_dwordx4 v2, s[32:33] offset:1152
	s_add_i32 m0, s26, 88960
	s_nop 0
	global_load_lds_dwordx4 v2, s[34:35] offset:1152
	s_add_i32 m0, s26, 89984
	s_nop 0
	global_load_lds_dwordx4 v2, s[36:37] offset:1152
	s_add_i32 m0, s26, 91008
	s_nop 0
	global_load_lds_dwordx4 v2, s[38:39] offset:1152
	s_add_i32 m0, s26, 92032
	s_nop 0
	global_load_lds_dwordx4 v2, s[40:41] offset:1152
	s_add_i32 m0, s26, 93056
	s_nop 0
	global_load_lds_dwordx4 v2, s[42:43] offset:1152
	s_waitcnt vmcnt(21)
	s_barrier
	s_add_i32 m0, s26, 115520
	s_nop 0
	global_load_lds_dwordx4 v2, s[30:31] offset:1216
	s_add_i32 m0, s26, 116544
	s_nop 0
	global_load_lds_dwordx4 v2, s[32:33] offset:1216
	s_add_i32 m0, s26, 117568
	s_nop 0
	global_load_lds_dwordx4 v2, s[34:35] offset:1216
	s_add_i32 m0, s26, 118592
	s_nop 0
	global_load_lds_dwordx4 v2, s[36:37] offset:1216
	s_add_i32 m0, s26, 119616
	s_nop 0
	global_load_lds_dwordx4 v2, s[38:39] offset:1216
	s_add_i32 m0, s26, 120640
	s_nop 0
	global_load_lds_dwordx4 v2, s[40:41] offset:1216
	s_add_i32 m0, s26, 121664
	s_nop 0
	global_load_lds_dwordx4 v2, s[42:43] offset:1216
	s_waitcnt vmcnt(21)
	s_barrier
	s_add_i32 m0, s26, 768
	s_nop 0
	global_load_lds_dwordx4 v2, s[30:31] offset:1280
	s_add_i32 m0, s26, 1792
	s_nop 0
	global_load_lds_dwordx4 v2, s[32:33] offset:1280
	s_add_i32 m0, s26, 2816
	s_nop 0
	global_load_lds_dwordx4 v2, s[34:35] offset:1280
	s_add_i32 m0, s26, 3840
	s_nop 0
	global_load_lds_dwordx4 v2, s[36:37] offset:1280
	s_add_i32 m0, s26, 4864
	s_nop 0
	global_load_lds_dwordx4 v2, s[38:39] offset:1280
	s_add_i32 m0, s26, 5888
	s_nop 0
	global_load_lds_dwordx4 v2, s[40:41] offset:1280
	s_add_i32 m0, s26, 6912
	s_nop 0
	global_load_lds_dwordx4 v2, s[42:43] offset:1280
	s_waitcnt vmcnt(21)
	s_barrier
	s_add_i32 m0, s26, 29376
	s_nop 0
	global_load_lds_dwordx4 v2, s[30:31] offset:1344
	s_add_i32 m0, s26, 30400
	s_nop 0
	global_load_lds_dwordx4 v2, s[32:33] offset:1344
	s_add_i32 m0, s26, 31424
	s_nop 0
	global_load_lds_dwordx4 v2, s[34:35] offset:1344
	s_add_i32 m0, s26, 32448
	s_nop 0
	global_load_lds_dwordx4 v2, s[36:37] offset:1344
	s_add_i32 m0, s26, 33472
	s_nop 0
	global_load_lds_dwordx4 v2, s[38:39] offset:1344
	s_add_i32 m0, s26, 34496
	s_nop 0
	global_load_lds_dwordx4 v2, s[40:41] offset:1344
	s_add_i32 m0, s26, 35520
	s_nop 0
	global_load_lds_dwordx4 v2, s[42:43] offset:1344
	s_waitcnt vmcnt(21)
	s_barrier
	s_add_i32 m0, s26, 57984
	s_nop 0
	global_load_lds_dwordx4 v2, s[30:31] offset:1408
	s_add_i32 m0, s26, 59008
	s_nop 0
	global_load_lds_dwordx4 v2, s[32:33] offset:1408
	s_add_i32 m0, s26, 60032
	s_nop 0
	global_load_lds_dwordx4 v2, s[34:35] offset:1408
	s_add_i32 m0, s26, 61056
	s_nop 0
	global_load_lds_dwordx4 v2, s[36:37] offset:1408
	s_add_i32 m0, s26, 62080
	s_nop 0
	global_load_lds_dwordx4 v2, s[38:39] offset:1408
	s_add_i32 m0, s26, 63104
	s_nop 0
	global_load_lds_dwordx4 v2, s[40:41] offset:1408
	s_add_i32 m0, s26, 64128
	s_nop 0
	global_load_lds_dwordx4 v2, s[42:43] offset:1408
	s_waitcnt vmcnt(21)
	s_barrier
	s_add_i32 m0, s26, 86592
	s_nop 0
	global_load_lds_dwordx4 v2, s[30:31] offset:1472
	s_add_i32 m0, s26, 87616
	s_nop 0
	global_load_lds_dwordx4 v2, s[32:33] offset:1472
	s_add_i32 m0, s26, 88640
	s_nop 0
	global_load_lds_dwordx4 v2, s[34:35] offset:1472
	s_add_i32 m0, s26, 89664
	s_nop 0
	global_load_lds_dwordx4 v2, s[36:37] offset:1472
	s_add_i32 m0, s26, 90688
	s_nop 0
	global_load_lds_dwordx4 v2, s[38:39] offset:1472
	s_add_i32 m0, s26, 91712
	s_nop 0
	global_load_lds_dwordx4 v2, s[40:41] offset:1472
	s_add_i32 m0, s26, 92736
	s_nop 0
	global_load_lds_dwordx4 v2, s[42:43] offset:1472
	s_waitcnt vmcnt(21)
	s_barrier
	s_waitcnt vmcnt(14)
	s_barrier
	s_waitcnt vmcnt(7)
	s_barrier
	s_waitcnt vmcnt(0)
	s_barrier

.LBB1_35:
	s_andn2_b64 vcc, exec, s[4:5]
	s_waitcnt vmcnt(0) lgkmcnt(0)
	s_barrier
	s_cbranch_vccnz .LBB1_108
	s_cmp_lt_u32 s2, 64
	s_cbranch_scc1 .Lqkv_tr_v
	v_mul_u32_u24_e32 v101, 0x190, v100
	v_lshlrev_b32_e32 v102, 3, v98
	v_add_u32_e32 v101, v101, v102
	s_lshl_b32 s6, s24, 1
	v_add_u32_e32 v101, s6, v101
	v_lshlrev_b32_e32 v103, 4, v98
	s_lshl_b32 s6, s24, 2
	s_add_i32 s6, s6, 0x23800
	v_add_u32_e32 v103, s6, v103
	ds_read_b128 v[104:107], v103
	ds_read_b128 v[108:111], v103 offset:32
	ds_read_b128 v[112:115], v103 offset:64
	ds_read_b128 v[116:119], v103 offset:96
	ds_read_b128 v[120:123], v103 offset:128
	ds_read_b128 v[124:127], v103 offset:160
	ds_read_b128 v[128:131], v103 offset:192
	ds_read_b128 v[132:135], v103 offset:224
	ds_read_b128 v[136:139], v103 offset:256
	ds_read_b128 v[140:143], v103 offset:288
	ds_read_b128 v[144:147], v103 offset:320
	ds_read_b128 v[148:151], v103 offset:352
	s_cmp_eq_u32 s3, 2
	s_cselect_b32 s19, 0x3e38aa3b, 1.0
	s_waitcnt lgkmcnt(0)
	v_fma_f32 v82, v82, s19, v104
	v_fma_f32 v83, v83, s19, v105
	v_fma_f32 v84, v84, s19, v106
	v_fma_f32 v85, v85, s19, v107
	v_cvt_pk_f16_f32 v82, v82, v83
	v_cvt_pk_f16_f32 v83, v84, v85
	ds_write_b64 v101, v[82:83]
	v_fma_f32 v86, v86, s19, v108
	v_fma_f32 v87, v87, s19, v109
	v_fma_f32 v88, v88, s19, v110
	v_fma_f32 v89, v89, s19, v111
	v_cvt_pk_f16_f32 v86, v86, v87
	v_cvt_pk_f16_f32 v87, v88, v89
	ds_write_b64 v101, v[86:87] offset:16
	v_fma_f32 v90, v90, s19, v112
	v_fma_f32 v91, v91, s19, v113
	v_fma_f32 v92, v92, s19, v114
	v_fma_f32 v93, v93, s19, v115
	v_cvt_pk_f16_f32 v90, v90, v91
	v_cvt_pk_f16_f32 v91, v92, v93
	ds_write_b64 v101, v[90:91] offset:32
	v_fma_f32 v94, v94, s19, v116
	v_fma_f32 v95, v95, s19, v117
	v_fma_f32 v96, v96, s19, v118
	v_fma_f32 v97, v97, s19, v119
	v_cvt_pk_f16_f32 v94, v94, v95
	v_cvt_pk_f16_f32 v95, v96, v97
	ds_write_b64 v101, v[94:95] offset:48
	v_fma_f32 v66, v66, s19, v120
	v_fma_f32 v67, v67, s19, v121
	v_fma_f32 v68, v68, s19, v122
	v_fma_f32 v69, v69, s19, v123
	v_cvt_pk_f16_f32 v66, v66, v67
	v_cvt_pk_f16_f32 v67, v68, v69
	ds_write_b64 v101, v[66:67] offset:64
	v_fma_f32 v70, v70, s19, v124
	v_fma_f32 v71, v71, s19, v125
	v_fma_f32 v72, v72, s19, v126
	v_fma_f32 v73, v73, s19, v127
	v_cvt_pk_f16_f32 v70, v70, v71
	v_cvt_pk_f16_f32 v71, v72, v73
	ds_write_b64 v101, v[70:71] offset:80
	v_fma_f32 v74, v74, s19, v128
	v_fma_f32 v75, v75, s19, v129
	v_fma_f32 v76, v76, s19, v130
	v_fma_f32 v77, v77, s19, v131
	v_cvt_pk_f16_f32 v74, v74, v75
	v_cvt_pk_f16_f32 v75, v76, v77
	ds_write_b64 v101, v[74:75] offset:96
	v_fma_f32 v78, v78, s19, v132
	v_fma_f32 v79, v79, s19, v133
	v_fma_f32 v80, v80, s19, v134
	v_fma_f32 v81, v81, s19, v135
	v_cvt_pk_f16_f32 v78, v78, v79
	v_cvt_pk_f16_f32 v79, v80, v81
	ds_write_b64 v101, v[78:79] offset:112
	v_fma_f32 v50, v50, s19, v136
	v_fma_f32 v51, v51, s19, v137
	v_fma_f32 v52, v52, s19, v138
	v_fma_f32 v53, v53, s19, v139
	v_cvt_pk_f16_f32 v50, v50, v51
	v_cvt_pk_f16_f32 v51, v52, v53
	ds_write_b64 v101, v[50:51] offset:128
	v_fma_f32 v54, v54, s19, v140
	v_fma_f32 v55, v55, s19, v141
	v_fma_f32 v56, v56, s19, v142
	v_fma_f32 v57, v57, s19, v143
	v_cvt_pk_f16_f32 v54, v54, v55
	v_cvt_pk_f16_f32 v55, v56, v57
	ds_write_b64 v101, v[54:55] offset:144
	v_fma_f32 v58, v58, s19, v144
	v_fma_f32 v59, v59, s19, v145
	v_fma_f32 v60, v60, s19, v146
	v_fma_f32 v61, v61, s19, v147
	v_cvt_pk_f16_f32 v58, v58, v59
	v_cvt_pk_f16_f32 v59, v60, v61
	ds_write_b64 v101, v[58:59] offset:160
	v_fma_f32 v62, v62, s19, v148
	v_fma_f32 v63, v63, s19, v149
	v_fma_f32 v64, v64, s19, v150
	v_fma_f32 v65, v65, s19, v151
	v_cvt_pk_f16_f32 v62, v62, v63
	v_cvt_pk_f16_f32 v63, v64, v65
	ds_write_b64 v101, v[62:63] offset:176
	v_fma_f32 v34, v34, s19, v104
	v_fma_f32 v35, v35, s19, v105
	v_fma_f32 v36, v36, s19, v106
	v_fma_f32 v37, v37, s19, v107
	v_cvt_pk_f16_f32 v34, v34, v35
	v_cvt_pk_f16_f32 v35, v36, v37
	ds_write_b64 v101, v[34:35] offset:12800
	v_fma_f32 v38, v38, s19, v108
	v_fma_f32 v39, v39, s19, v109
	v_fma_f32 v40, v40, s19, v110
	v_fma_f32 v41, v41, s19, v111
	v_cvt_pk_f16_f32 v38, v38, v39
	v_cvt_pk_f16_f32 v39, v40, v41
	ds_write_b64 v101, v[38:39] offset:12816
	v_fma_f32 v42, v42, s19, v112
	v_fma_f32 v43, v43, s19, v113
	v_fma_f32 v44, v44, s19, v114
	v_fma_f32 v45, v45, s19, v115
	v_cvt_pk_f16_f32 v42, v42, v43
	v_cvt_pk_f16_f32 v43, v44, v45
	ds_write_b64 v101, v[42:43] offset:12832
	v_fma_f32 v46, v46, s19, v116
	v_fma_f32 v47, v47, s19, v117
	v_fma_f32 v48, v48, s19, v118
	v_fma_f32 v49, v49, s19, v119
	v_cvt_pk_f16_f32 v46, v46, v47
	v_cvt_pk_f16_f32 v47, v48, v49
	ds_write_b64 v101, v[46:47] offset:12848
	v_fma_f32 v18, v18, s19, v120
	v_fma_f32 v19, v19, s19, v121
	v_fma_f32 v20, v20, s19, v122
	v_fma_f32 v21, v21, s19, v123
	v_cvt_pk_f16_f32 v18, v18, v19
	v_cvt_pk_f16_f32 v19, v20, v21
	ds_write_b64 v101, v[18:19] offset:12864
	v_fma_f32 v22, v22, s19, v124
	v_fma_f32 v23, v23, s19, v125
	v_fma_f32 v24, v24, s19, v126
	v_fma_f32 v25, v25, s19, v127
	v_cvt_pk_f16_f32 v22, v22, v23
	v_cvt_pk_f16_f32 v23, v24, v25
	ds_write_b64 v101, v[22:23] offset:12880
	v_fma_f32 v26, v26, s19, v128
	v_fma_f32 v27, v27, s19, v129
	v_fma_f32 v28, v28, s19, v130
	v_fma_f32 v29, v29, s19, v131
	v_cvt_pk_f16_f32 v26, v26, v27
	v_cvt_pk_f16_f32 v27, v28, v29
	ds_write_b64 v101, v[26:27] offset:12896
	v_fma_f32 v30, v30, s19, v132
	v_fma_f32 v31, v31, s19, v133
	v_fma_f32 v32, v32, s19, v134
	v_fma_f32 v33, v33, s19, v135
	v_cvt_pk_f16_f32 v30, v30, v31
	v_cvt_pk_f16_f32 v31, v32, v33
	ds_write_b64 v101, v[30:31] offset:12912
	v_fma_f32 v2, v2, s19, v136
	v_fma_f32 v3, v3, s19, v137
	v_fma_f32 v4, v4, s19, v138
	v_fma_f32 v5, v5, s19, v139
	v_cvt_pk_f16_f32 v2, v2, v3
	v_cvt_pk_f16_f32 v3, v4, v5
	ds_write_b64 v101, v[2:3] offset:12928
	v_fma_f32 v6, v6, s19, v140
	v_fma_f32 v7, v7, s19, v141
	v_fma_f32 v8, v8, s19, v142
	v_fma_f32 v9, v9, s19, v143
	v_cvt_pk_f16_f32 v6, v6, v7
	v_cvt_pk_f16_f32 v7, v8, v9
	ds_write_b64 v101, v[6:7] offset:12944
	v_fma_f32 v10, v10, s19, v144
	v_fma_f32 v11, v11, s19, v145
	v_fma_f32 v12, v12, s19, v146
	v_fma_f32 v13, v13, s19, v147
	v_cvt_pk_f16_f32 v10, v10, v11
	v_cvt_pk_f16_f32 v11, v12, v13
	ds_write_b64 v101, v[10:11] offset:12960
	v_fma_f32 v14, v14, s19, v148
	v_fma_f32 v15, v15, s19, v149
	v_fma_f32 v16, v16, s19, v150
	v_fma_f32 v17, v17, s19, v151
	v_cvt_pk_f16_f32 v14, v14, v15
	v_cvt_pk_f16_f32 v15, v16, v17
	ds_write_b64 v101, v[14:15] offset:12976
	s_branch .LBB1_108
.Lqkv_tr_v:
	v_mul_u32_u24_e32 v101, 0x210, v99
	v_lshlrev_b32_e32 v102, 3, v98
	v_add_u32_e32 v101, v101, v102
	s_lshl_b32 s6, s23, 1
	v_add_u32_e32 v101, s6, v101
	s_lshl_b32 s6, s24, 2
	s_add_i32 s6, s6, 0x23800
	v_lshl_add_u32 v103, v1, 2, s6
	ds_read_b32 v104, v103
	ds_read_b32 v105, v103 offset:128
	ds_read_b32 v106, v103 offset:256
	s_waitcnt lgkmcnt(0)
	v_add_f32_e32 v82, v82, v104
	v_add_f32_e32 v83, v83, v104
	v_add_f32_e32 v84, v84, v104
	v_add_f32_e32 v85, v85, v104
	v_cvt_pk_f16_f32 v82, v82, v83
	v_cvt_pk_f16_f32 v83, v84, v85
	ds_write_b64 v101, v[82:83]
	v_add_f32_e32 v86, v86, v104
	v_add_f32_e32 v87, v87, v104
	v_add_f32_e32 v88, v88, v104
	v_add_f32_e32 v89, v89, v104
	v_cvt_pk_f16_f32 v86, v86, v87
	v_cvt_pk_f16_f32 v87, v88, v89
	ds_write_b64 v101, v[86:87] offset:16
	v_add_f32_e32 v90, v90, v104
	v_add_f32_e32 v91, v91, v104
	v_add_f32_e32 v92, v92, v104
	v_add_f32_e32 v93, v93, v104
	v_cvt_pk_f16_f32 v90, v90, v91
	v_cvt_pk_f16_f32 v91, v92, v93
	ds_write_b64 v101, v[90:91] offset:32
	v_add_f32_e32 v94, v94, v104
	v_add_f32_e32 v95, v95, v104
	v_add_f32_e32 v96, v96, v104
	v_add_f32_e32 v97, v97, v104
	v_cvt_pk_f16_f32 v94, v94, v95
	v_cvt_pk_f16_f32 v95, v96, v97
	ds_write_b64 v101, v[94:95] offset:48
	v_add_f32_e32 v34, v34, v104
	v_add_f32_e32 v35, v35, v104
	v_add_f32_e32 v36, v36, v104
	v_add_f32_e32 v37, v37, v104
	v_cvt_pk_f16_f32 v34, v34, v35
	v_cvt_pk_f16_f32 v35, v36, v37
	ds_write_b64 v101, v[34:35] offset:64
	v_add_f32_e32 v38, v38, v104
	v_add_f32_e32 v39, v39, v104
	v_add_f32_e32 v40, v40, v104
	v_add_f32_e32 v41, v41, v104
	v_cvt_pk_f16_f32 v38, v38, v39
	v_cvt_pk_f16_f32 v39, v40, v41
	ds_write_b64 v101, v[38:39] offset:80
	v_add_f32_e32 v42, v42, v104
	v_add_f32_e32 v43, v43, v104
	v_add_f32_e32 v44, v44, v104
	v_add_f32_e32 v45, v45, v104
	v_cvt_pk_f16_f32 v42, v42, v43
	v_cvt_pk_f16_f32 v43, v44, v45
	ds_write_b64 v101, v[42:43] offset:96
	v_add_f32_e32 v46, v46, v104
	v_add_f32_e32 v47, v47, v104
	v_add_f32_e32 v48, v48, v104
	v_add_f32_e32 v49, v49, v104
	v_cvt_pk_f16_f32 v46, v46, v47
	v_cvt_pk_f16_f32 v47, v48, v49
	ds_write_b64 v101, v[46:47] offset:112
	v_add_f32_e32 v66, v66, v105
	v_add_f32_e32 v67, v67, v105
	v_add_f32_e32 v68, v68, v105
	v_add_f32_e32 v69, v69, v105
	v_cvt_pk_f16_f32 v66, v66, v67
	v_cvt_pk_f16_f32 v67, v68, v69
	ds_write_b64 v101, v[66:67] offset:16896
	v_add_f32_e32 v70, v70, v105
	v_add_f32_e32 v71, v71, v105
	v_add_f32_e32 v72, v72, v105
	v_add_f32_e32 v73, v73, v105
	v_cvt_pk_f16_f32 v70, v70, v71
	v_cvt_pk_f16_f32 v71, v72, v73
	ds_write_b64 v101, v[70:71] offset:16912
	v_add_f32_e32 v74, v74, v105
	v_add_f32_e32 v75, v75, v105
	v_add_f32_e32 v76, v76, v105
	v_add_f32_e32 v77, v77, v105
	v_cvt_pk_f16_f32 v74, v74, v75
	v_cvt_pk_f16_f32 v75, v76, v77
	ds_write_b64 v101, v[74:75] offset:16928
	v_add_f32_e32 v78, v78, v105
	v_add_f32_e32 v79, v79, v105
	v_add_f32_e32 v80, v80, v105
	v_add_f32_e32 v81, v81, v105
	v_cvt_pk_f16_f32 v78, v78, v79
	v_cvt_pk_f16_f32 v79, v80, v81
	ds_write_b64 v101, v[78:79] offset:16944
	v_add_f32_e32 v18, v18, v105
	v_add_f32_e32 v19, v19, v105
	v_add_f32_e32 v20, v20, v105
	v_add_f32_e32 v21, v21, v105
	v_cvt_pk_f16_f32 v18, v18, v19
	v_cvt_pk_f16_f32 v19, v20, v21
	ds_write_b64 v101, v[18:19] offset:16960
	v_add_f32_e32 v22, v22, v105
	v_add_f32_e32 v23, v23, v105
	v_add_f32_e32 v24, v24, v105
	v_add_f32_e32 v25, v25, v105
	v_cvt_pk_f16_f32 v22, v22, v23
	v_cvt_pk_f16_f32 v23, v24, v25
	ds_write_b64 v101, v[22:23] offset:16976
	v_add_f32_e32 v26, v26, v105
	v_add_f32_e32 v27, v27, v105
	v_add_f32_e32 v28, v28, v105
	v_add_f32_e32 v29, v29, v105
	v_cvt_pk_f16_f32 v26, v26, v27
	v_cvt_pk_f16_f32 v27, v28, v29
	ds_write_b64 v101, v[26:27] offset:16992
	v_add_f32_e32 v30, v30, v105
	v_add_f32_e32 v31, v31, v105
	v_add_f32_e32 v32, v32, v105
	v_add_f32_e32 v33, v33, v105
	v_cvt_pk_f16_f32 v30, v30, v31
	v_cvt_pk_f16_f32 v31, v32, v33
	ds_write_b64 v101, v[30:31] offset:17008
	v_add_f32_e32 v50, v50, v106
	v_add_f32_e32 v51, v51, v106
	v_add_f32_e32 v52, v52, v106
	v_add_f32_e32 v53, v53, v106
	v_cvt_pk_f16_f32 v50, v50, v51
	v_cvt_pk_f16_f32 v51, v52, v53
	ds_write_b64 v101, v[50:51] offset:33792
	v_add_f32_e32 v54, v54, v106
	v_add_f32_e32 v55, v55, v106
	v_add_f32_e32 v56, v56, v106
	v_add_f32_e32 v57, v57, v106
	v_cvt_pk_f16_f32 v54, v54, v55
	v_cvt_pk_f16_f32 v55, v56, v57
	ds_write_b64 v101, v[54:55] offset:33808
	v_add_f32_e32 v58, v58, v106
	v_add_f32_e32 v59, v59, v106
	v_add_f32_e32 v60, v60, v106
	v_add_f32_e32 v61, v61, v106
	v_cvt_pk_f16_f32 v58, v58, v59
	v_cvt_pk_f16_f32 v59, v60, v61
	ds_write_b64 v101, v[58:59] offset:33824
	v_add_f32_e32 v62, v62, v106
	v_add_f32_e32 v63, v63, v106
	v_add_f32_e32 v64, v64, v106
	v_add_f32_e32 v65, v65, v106
	v_cvt_pk_f16_f32 v62, v62, v63
	v_cvt_pk_f16_f32 v63, v64, v65
	ds_write_b64 v101, v[62:63] offset:33840
	v_add_f32_e32 v2, v2, v106
	v_add_f32_e32 v3, v3, v106
	v_add_f32_e32 v4, v4, v106
	v_add_f32_e32 v5, v5, v106
	v_cvt_pk_f16_f32 v2, v2, v3
	v_cvt_pk_f16_f32 v3, v4, v5
	ds_write_b64 v101, v[2:3] offset:33856
	v_add_f32_e32 v6, v6, v106
	v_add_f32_e32 v7, v7, v106
	v_add_f32_e32 v8, v8, v106
	v_add_f32_e32 v9, v9, v106
	v_cvt_pk_f16_f32 v6, v6, v7
	v_cvt_pk_f16_f32 v7, v8, v9
	ds_write_b64 v101, v[6:7] offset:33872
	v_add_f32_e32 v10, v10, v106
	v_add_f32_e32 v11, v11, v106
	v_add_f32_e32 v12, v12, v106
	v_add_f32_e32 v13, v13, v106
	v_cvt_pk_f16_f32 v10, v10, v11
	v_cvt_pk_f16_f32 v11, v12, v13
	ds_write_b64 v101, v[10:11] offset:33888
	v_add_f32_e32 v14, v14, v106
	v_add_f32_e32 v15, v15, v106
	v_add_f32_e32 v16, v16, v106
	v_add_f32_e32 v17, v17, v106
	v_cvt_pk_f16_f32 v14, v14, v15
	v_cvt_pk_f16_f32 v15, v16, v17
	ds_write_b64 v101, v[14:15] offset:33904
.LBB1_108:
	s_load_dwordx2 s[24:25], s[0:1], 0x38
	s_cmp_eq_u32 s3, 1
	s_cselect_b32 s6, s16, s14
	s_cselect_b32 s7, s17, s15
	s_lshr_b32 s23, s22, 3
	s_and_b32 s26, s21, 0x700
	s_waitcnt lgkmcnt(0)
	s_barrier
	s_cmp_lt_u32 s2, 64
	s_cbranch_scc1 .Lqkv_out_v
	s_mov_b32 s27, 0xaaaaaab
	v_mul_hi_u32 v1, v0, s27
	v_mul_u32_u24_e32 v2, 24, v1
	v_sub_u32_e32 v2, v0, v2
	v_lshl_add_u32 v3, v2, 3, s20
	v_mul_u32_u24_e32 v5, 0x190, v1
	v_lshl_add_u32 v5, v2, 4, v5
	v_add_u32_e32 v6, 0xc800, v5
	ds_read_b128 v[16:19], v5
	ds_read_b128 v[20:23], v5 offset:12800
	ds_read_b128 v[24:27], v5 offset:25600
	ds_read_b128 v[28:31], v5 offset:38400
	ds_read_b128 v[32:35], v6
	ds_read_b128 v[36:39], v6 offset:12800
	ds_read_b128 v[40:43], v6 offset:25600
	ds_read_b128 v[44:47], v6 offset:38400
	v_lshrrev_b32_e32 v7, 6, v3
	s_mul_i32 s27, s23, 12
	v_add_u32_e32 v7, s27, v7
	v_lshlrev_b32_e32 v7, 18, v7
	v_and_b32_e32 v48, 63, v3
	v_lshlrev_b32_e32 v48, 1, v48
	v_add_u32_e32 v49, s26, v1
	v_lshl_add_u32 v48, v49, 7, v48
	v_add_u32_e32 v7, v7, v48
	s_waitcnt lgkmcnt(7)
	global_store_dwordx4 v7, v[16:19], s[6:7]
	v_add_u32_e32 v7, 0x1000, v7
	s_waitcnt lgkmcnt(6)
	global_store_dwordx4 v7, v[20:23], s[6:7]
	v_add_u32_e32 v7, 0x1000, v7
	s_waitcnt lgkmcnt(5)
	global_store_dwordx4 v7, v[24:27], s[6:7]
	v_add_u32_e32 v7, 0x1000, v7
	s_waitcnt lgkmcnt(4)
	global_store_dwordx4 v7, v[28:31], s[6:7]
	v_add_u32_e32 v7, 0x1000, v7
	s_waitcnt lgkmcnt(3)
	global_store_dwordx4 v7, v[32:35], s[6:7]
	v_add_u32_e32 v7, 0x1000, v7
	s_waitcnt lgkmcnt(2)
	global_store_dwordx4 v7, v[36:39], s[6:7]
	v_add_u32_e32 v7, 0x1000, v7
	s_waitcnt lgkmcnt(1)
	global_store_dwordx4 v7, v[40:43], s[6:7]
	v_add_u32_e32 v7, 0x1000, v7
	s_waitcnt lgkmcnt(0)
	global_store_dwordx4 v7, v[44:47], s[6:7]
	s_endpgm
.Lqkv_out_v:
	v_lshrrev_b32_e32 v1, 5, v0
	v_and_b32_e32 v2, 31, v0
	v_add_u32_e32 v3, s20, v1
	v_mul_u32_u24_e32 v5, 0x210, v1
	v_lshl_add_u32 v5, v2, 4, v5
	v_add_u32_e32 v6, 0xc600, v5
	ds_read_b128 v[16:19], v5
	ds_read_b128 v[20:23], v5 offset:12672
	ds_read_b128 v[24:27], v5 offset:25344
	ds_read_b128 v[28:31], v5 offset:38016
	ds_read_b128 v[32:35], v6
	ds_read_b128 v[36:39], v6 offset:12672
	ds_read_b128 v[40:43], v6 offset:25344
	ds_read_b128 v[44:47], v6 offset:38016
	s_mul_i32 s27, s23, 0x300
	v_add_u32_e32 v7, s27, v3
	v_lshlrev_b32_e32 v7, 12, v7
	v_lshl_add_u32 v48, v2, 3, s26
	v_lshl_add_u32 v7, v48, 1, v7
	s_waitcnt lgkmcnt(7)
	global_store_dwordx4 v7, v[16:19], s[24:25]
	v_add_u32_e32 v7, 0x18000, v7
	s_waitcnt lgkmcnt(6)
	global_store_dwordx4 v7, v[20:23], s[24:25]
	v_add_u32_e32 v7, 0x18000, v7
	s_waitcnt lgkmcnt(5)
	global_store_dwordx4 v7, v[24:27], s[24:25]
	v_add_u32_e32 v7, 0x18000, v7
	s_waitcnt lgkmcnt(4)
	global_store_dwordx4 v7, v[28:31], s[24:25]
	v_add_u32_e32 v7, 0x18000, v7
	s_waitcnt lgkmcnt(3)
	global_store_dwordx4 v7, v[32:35], s[24:25]
	v_add_u32_e32 v7, 0x18000, v7
	s_waitcnt lgkmcnt(2)
	global_store_dwordx4 v7, v[36:39], s[24:25]
	v_add_u32_e32 v7, 0x18000, v7
	s_waitcnt lgkmcnt(1)
	global_store_dwordx4 v7, v[40:43], s[24:25]
	v_add_u32_e32 v7, 0x18000, v7
	s_waitcnt lgkmcnt(0)
	global_store_dwordx4 v7, v[44:47], s[24:25]
	s_endpgm

	.amdhsa_kernel _Z15qkv_proj_kernelPKDF16_S0_PKfS2_S2_PDF16_S3_S3_
		.amdhsa_group_segment_fixed_size 31744
		.amdhsa_private_segment_fixed_size 0
		.amdhsa_kernarg_size 64
		.amdhsa_user_sgpr_count 2
		.amdhsa_user_sgpr_dispatch_ptr 0
		.amdhsa_user_sgpr_queue_ptr 0
		.amdhsa_user_sgpr_kernarg_segment_ptr 1
		.amdhsa_user_sgpr_dispatch_id 0
		.amdhsa_user_sgpr_kernarg_preload_length 0
		.amdhsa_user_sgpr_kernarg_preload_offset 0
		.amdhsa_user_sgpr_private_segment_size 0
		.amdhsa_uses_dynamic_stack 0
		.amdhsa_enable_private_segment 0
		.amdhsa_system_sgpr_workgroup_id_x 1
		.amdhsa_system_sgpr_workgroup_id_y 0
		.amdhsa_system_sgpr_workgroup_id_z 0
		.amdhsa_system_sgpr_workgroup_info 0
		.amdhsa_system_vgpr_workitem_id 0
		.amdhsa_next_free_vgpr 156
		.amdhsa_next_free_sgpr 46
		.amdhsa_accum_offset 156
		.amdhsa_reserve_vcc 1
		.amdhsa_float_round_mode_32 0
		.amdhsa_float_round_mode_16_64 0
		.amdhsa_float_denorm_mode_32 3
		.amdhsa_float_denorm_mode_16_64 3
		.amdhsa_dx10_clamp 1
		.amdhsa_ieee_mode 1
		.amdhsa_fp16_overflow 0
		.amdhsa_tg_split 0
		.amdhsa_exception_fp_ieee_invalid_op 0
		.amdhsa_exception_fp_denorm_src 0
		.amdhsa_exception_fp_ieee_div_zero 0
		.amdhsa_exception_fp_ieee_overflow 0
		.amdhsa_exception_fp_ieee_underflow 0
		.amdhsa_exception_fp_ieee_inexact 0
		.amdhsa_exception_int_div_zero 0
	.end_amdhsa_kernel

amdhsa.kernels:
  - .agpr_count:     0
    .args:
      - .actual_access:  read_only
        .address_space:  global
        .offset:         0
        .size:           8
        .value_kind:     global_buffer
      - .actual_access:  read_only
        .address_space:  global
        .offset:         8
        .size:           8
        .value_kind:     global_buffer
      - .actual_access:  read_only
        .address_space:  global
        .offset:         16
        .size:           8
        .value_kind:     global_buffer
      - .actual_access:  read_only
        .address_space:  global
        .offset:         24
        .size:           8
        .value_kind:     global_buffer
      - .actual_access:  read_only
        .address_space:  global
        .offset:         32
        .size:           8
        .value_kind:     global_buffer
      - .actual_access:  read_only
        .address_space:  global
        .offset:         40
        .size:           8
        .value_kind:     global_buffer
      - .actual_access:  read_only
        .address_space:  global
        .offset:         48
        .size:           8
        .value_kind:     global_buffer
      - .actual_access:  write_only
        .address_space:  global
        .offset:         56
        .size:           8
        .value_kind:     global_buffer
      - .actual_access:  write_only
        .address_space:  global
        .offset:         64
        .size:           8
        .value_kind:     global_buffer
    .group_segment_fixed_size: 0
    .kernarg_segment_align: 8
    .kernarg_segment_size: 72
    .language:       OpenCL C
    .language_version:
      - 2
      - 0
    .max_flat_workgroup_size: 256
    .name:           _Z11prep_kernelPKfS0_S0_S0_S0_S0_S0_PDF16_S1_
    .private_segment_fixed_size: 0
    .sgpr_count:     21
    .sgpr_spill_count: 0
    .symbol:         _Z11prep_kernelPKfS0_S0_S0_S0_S0_S0_PDF16_S1_.kd
    .uniform_work_group_size: 1
    .uses_dynamic_stack: false
    .vgpr_count:     10
    .vgpr_spill_count: 0
    .wavefront_size: 64
  - .agpr_count:     0
    .args:
      - .address_space:  global
        .offset:         0
        .size:           8
        .value_kind:     global_buffer
      - .address_space:  global
        .offset:         8
        .size:           8
        .value_kind:     global_buffer
      - .actual_access:  read_only
        .address_space:  global
        .offset:         16
        .size:           8
        .value_kind:     global_buffer
      - .actual_access:  read_only
        .address_space:  global
        .offset:         24
        .size:           8
        .value_kind:     global_buffer
      - .actual_access:  read_only
        .address_space:  global
        .offset:         32
        .size:           8
        .value_kind:     global_buffer
      - .actual_access:  write_only
        .address_space:  global
        .offset:         40
        .size:           8
        .value_kind:     global_buffer
      - .actual_access:  write_only
        .address_space:  global
        .offset:         48
        .size:           8
        .value_kind:     global_buffer
      - .actual_access:  write_only
        .address_space:  global
        .offset:         56
        .size:           8
        .value_kind:     global_buffer
    .group_segment_fixed_size: 31744
    .kernarg_segment_align: 8
    .kernarg_segment_size: 64
    .language:       OpenCL C
    .language_version:
      - 2
      - 0
    .max_flat_workgroup_size: 768
    .name:           _Z15qkv_proj_kernelPKDF16_S0_PKfS2_S2_PDF16_S3_S3_
    .private_segment_fixed_size: 0
    .sgpr_count:     47
    .sgpr_spill_count: 0
    .symbol:         _Z15qkv_proj_kernelPKDF16_S0_PKfS2_S2_PDF16_S3_S3_.kd
    .uniform_work_group_size: 1
    .uses_dynamic_stack: false
    .vgpr_count:     156
    .vgpr_spill_count: 0
    .wavefront_size: 64
  - .agpr_count:     0
    .args:
      - .address_space:  global
        .offset:         0
        .size:           8
        .value_kind:     global_buffer
      - .address_space:  global
        .offset:         8
        .size:           8
        .value_kind:     global_buffer
      - .actual_access:  read_only
        .address_space:  global
        .offset:         16
        .size:           8
        .value_kind:     global_buffer
      - .actual_access:  write_only
        .address_space:  global
        .offset:         24
        .size:           8
        .value_kind:     global_buffer
    .group_segment_fixed_size: 30720
    .kernarg_segment_align: 8
    .kernarg_segment_size: 32
    .language:       OpenCL C
    .language_version:
      - 2
      - 0
    .max_flat_workgroup_size: 384
    .name:           _Z15out_proj_kernelPKDF16_S0_PKfPf
    .private_segment_fixed_size: 0
    .sgpr_count:     67
    .sgpr_spill_count: 0
    .symbol:         _Z15out_proj_kernelPKDF16_S0_PKfPf.kd
    .uniform_work_group_size: 1
    .uses_dynamic_stack: false
    .vgpr_count:     144
    .vgpr_spill_count: 0
    .wavefront_size: 64
  - .agpr_count:     0
    .args:
      - .actual_access:  read_only
        .address_space:  global
        .offset:         0
        .size:           8
        .value_kind:     global_buffer
      - .address_space:  global
        .offset:         8
        .size:           8
        .value_kind:     global_buffer
      - .address_space:  global
        .offset:         16
        .size:           8
        .value_kind:     global_buffer
      - .actual_access:  write_only
        .address_space:  global
        .offset:         24
        .size:           8
        .value_kind:     global_buffer
      - .actual_access:  write_only
        .address_space:  global
        .offset:         32
        .size:           8
        .value_kind:     global_buffer
    .group_segment_fixed_size: 49152
    .kernarg_segment_align: 8
    .kernarg_segment_size: 40
    .language:       OpenCL C
    .language_version:
      - 2
      - 0
    .max_flat_workgroup_size: 256
    .name:           _Z11attn_kernelPKDF16_S0_S0_PDF16_P15HIP_vector_typeIfLj2EE
    .private_segment_fixed_size: 0
    .sgpr_count:     34
    .sgpr_spill_count: 0
    .symbol:         _Z11attn_kernelPKDF16_S0_S0_PDF16_P15HIP_vector_typeIfLj2EE.kd
    .uniform_work_group_size: 1
    .uses_dynamic_stack: false
    .vgpr_count:     168
    .vgpr_spill_count: 0
    .wavefront_size: 64
  - .agpr_count:     0
    .args:
      - .actual_access:  read_only
        .address_space:  global
        .offset:         0
        .size:           8
        .value_kind:     global_buffer
      - .actual_access:  read_only
        .address_space:  global
        .offset:         8
        .size:           8
        .value_kind:     global_buffer
      - .actual_access:  write_only
        .address_space:  global
        .offset:         16
        .size:           8
        .value_kind:     global_buffer
    .group_segment_fixed_size: 0
    .kernarg_segment_align: 8
    .kernarg_segment_size: 24
    .language:       OpenCL C
    .language_version:
      - 2
      - 0
    .max_flat_workgroup_size: 256
    .name:           _Z14combine_kernelPKDF16_PK15HIP_vector_typeIfLj2EEPDF16_
    .private_segment_fixed_size: 0
    .sgpr_count:     16
    .sgpr_spill_count: 0
    .symbol:         _Z14combine_kernelPKDF16_PK15HIP_vector_typeIfLj2EEPDF16_.kd
    .uniform_work_group_size: 1
    .uses_dynamic_stack: false
    .vgpr_count:     44
    .vgpr_spill_count: 0
    .wavefront_size: 64
